# split the ml_out-internal grid barrier: unit prologue (gate loads, block scan) runs before the wait, which sits in front of the entering-state copy; on top of v72
# speedup vs baseline: 1.0093x; 1.0023x over previous
.LBB0_601:
	s_andn2_b64 vcc, exec, s[10:11]
	s_mov_b32 s46, s9
	s_cbranch_vccnz .LBB0_655
	s_waitcnt vmcnt(0)
	s_barrier
	s_mov_b64 s[10:11], exec
	v_readlane_b32 s44, v254, 12
	v_readlane_b32 s45, v254, 13
	s_and_b64 s[44:45], s[10:11], s[44:45]
	s_mov_b64 exec, s[44:45]
	s_cbranch_execz .LBB0_654
	v_mov_b32_e32 v7, 0x22160
	s_waitcnt vmcnt(0) lgkmcnt(0)
	ds_read_b32 v8, v7
	v_mov_b32_e32 v9, 1
	v_mov_b32_e32 v10, s99
	v_and_b32_e32 v11, 0xffff, v10
	v_lshrrev_b32_e32 v12, 16, v10
	global_atomic_add v13, v11, v9, s[100:101] sc0
	buffer_inv sc1
	v_lshrrev_b32_e32 v14, 8, v11
	v_sub_u32_e32 v14, s98, v14
	v_add_u32_e32 v14, 7, v14
	v_lshrrev_b32_e32 v14, 3, v14
	v_mov_b32_e32 v15, s98
	v_min_u32_e32 v15, 8, v15
	v_mov_b32_e32 v16, 0
	s_waitcnt lgkmcnt(0)
	v_add_u32_e32 v8, 1, v8
	ds_write_b32 v7, v8
	v_mul_lo_u32 v14, v14, v8
	v_mul_lo_u32 v15, v15, v8
	s_waitcnt vmcnt(0)
	v_add_u32_e32 v13, 1, v13
	v_cmp_eq_u32_e32 vcc, v13, v14
	s_cbranch_vccz .Lgb_done_3
	v_mov_b32_e32 v10, 0
	global_atomic_add v10, v9, s[100:101] offset:2048
	global_atomic_add v10, v9, s[100:101] offset:2304
	global_atomic_add v10, v9, s[100:101] offset:2560
	global_atomic_add v10, v9, s[100:101] offset:2816
	global_atomic_add v10, v9, s[100:101] offset:3072
	global_atomic_add v10, v9, s[100:101] offset:3328
	global_atomic_add v10, v9, s[100:101] offset:3584
	global_atomic_add v10, v9, s[100:101] offset:3840
.Lgb_done_3:
	s_waitcnt lgkmcnt(0)
.LBB0_654:
	s_or_b64 exec, exec, s[10:11]
	v_readlane_b32 s46, v254, 17
	s_waitcnt lgkmcnt(0)
.LBB0_655:
	s_xor_b64 s[10:11], s[12:13], -1
	s_cmp_lt_i32 s46, 0
	s_cbranch_scc1 .LBB0_600
	s_cmpk_lt_u32 s46, 0x100
	s_cselect_b64 s[12:13], -1, 0
	s_cmpk_gt_u32 s46, 0xff
	s_mov_b64 s[56:57], -1
	s_cbranch_scc0 .LBB0_658
	s_add_i32 s6, s46, 0xffffff00
	s_mov_b64 s[56:57], 0

.LBB0_683:
	s_or_b64 exec, exec, s[56:57]
	s_waitcnt vmcnt(0)
	v_cndmask_b32_e64 v8, 0, 1, s[12:13]
	v_cmp_ne_u32_e64 s[56:57], 1, v8
	s_andn2_b64 vcc, exec, s[12:13]
	s_mov_b32 s45, 1
	s_cbranch_vccnz .LBB0_687
	v_readlane_b32 s58, v254, 12
	v_readlane_b32 s59, v254, 13
	s_and_saveexec_b64 s[12:13], s[58:59]
	s_cbranch_execz .Lgw_end_3
	v_mov_b32_e32 v8, 0x22160
	ds_read_b32 v9, v8
	v_mov_b32_e32 v10, s99
	v_lshrrev_b32_e32 v11, 16, v10
	v_mov_b32_e32 v12, s98
	v_min_u32_e32 v12, 8, v12
	v_mov_b32_e32 v13, 0
	s_waitcnt lgkmcnt(0)
	v_mul_lo_u32 v12, v12, v9
.Lgw_poll_3:
	global_load_dword v14, v11, s[100:101] sc1
	v_add_u32_e32 v13, 1, v13
	s_waitcnt vmcnt(0)
	v_cmp_ge_u32_e32 vcc, v14, v12
	s_cbranch_vccnz .Lgw_end_3
	v_cmp_gt_u32_e32 vcc, 0x80000, v13
	s_sleep 1
	s_cbranch_vccnz .Lgw_poll_3
.Lgw_end_3:
	s_or_b64 exec, exec, s[12:13]
	s_barrier
	s_mul_i32 s12, s46, 0x11000
	v_readlane_b32 s13, v254, 15
	s_add_u32 s12, s13, s12
	v_readlane_b32 s13, v254, 16
	s_addc_u32 s13, s13, 0
	s_mov_b64 s[58:59], 0
	v_mov_b32_e32 v8, v0
	v_mov_b32_e32 v8, v0
	v_mul_u32_u24_e32 v9, 0xf0f1, v8
	v_lshrrev_b32_e32 v9, 21, v9
	v_mul_u32_u24_e32 v14, 34, v9
	v_sub_u32_e32 v14, v8, v14
	v_mul_u32_u24_e32 v10, 0x220, v9
	v_lshl_add_u32 v10, v14, 4, v10
	v_mul_u32_u24_e32 v9, 0x230, v9
	v_lshl_add_u32 v136, v14, 4, v9
	global_load_dwordx4 v[100:103], v10, s[12:13]
	v_add_u32_e32 v8, 0x200, v0
	v_mul_u32_u24_e32 v9, 0xf0f1, v8
	v_lshrrev_b32_e32 v9, 21, v9
	v_mul_u32_u24_e32 v14, 34, v9
	v_sub_u32_e32 v14, v8, v14
	v_mul_u32_u24_e32 v10, 0x220, v9
	v_lshl_add_u32 v10, v14, 4, v10
	v_mul_u32_u24_e32 v9, 0x230, v9
	v_lshl_add_u32 v137, v14, 4, v9
	global_load_dwordx4 v[104:107], v10, s[12:13]
	v_add_u32_e32 v8, 0x400, v0
	v_mul_u32_u24_e32 v9, 0xf0f1, v8
	v_lshrrev_b32_e32 v9, 21, v9
	v_mul_u32_u24_e32 v14, 34, v9
	v_sub_u32_e32 v14, v8, v14
	v_mul_u32_u24_e32 v10, 0x220, v9
	v_lshl_add_u32 v10, v14, 4, v10
	v_mul_u32_u24_e32 v9, 0x230, v9
	v_lshl_add_u32 v138, v14, 4, v9
	global_load_dwordx4 v[108:111], v10, s[12:13]
	v_add_u32_e32 v8, 0x600, v0
	v_mul_u32_u24_e32 v9, 0xf0f1, v8
	v_lshrrev_b32_e32 v9, 21, v9
	v_mul_u32_u24_e32 v14, 34, v9
	v_sub_u32_e32 v14, v8, v14
	v_mul_u32_u24_e32 v10, 0x220, v9
	v_lshl_add_u32 v10, v14, 4, v10
	v_mul_u32_u24_e32 v9, 0x230, v9
	v_lshl_add_u32 v139, v14, 4, v9
	global_load_dwordx4 v[112:115], v10, s[12:13]
	v_add_u32_e32 v8, 0x800, v0
	v_mul_u32_u24_e32 v9, 0xf0f1, v8
	v_lshrrev_b32_e32 v9, 21, v9
	v_mul_u32_u24_e32 v14, 34, v9
	v_sub_u32_e32 v14, v8, v14
	v_mul_u32_u24_e32 v10, 0x220, v9
	v_lshl_add_u32 v10, v14, 4, v10
	v_mul_u32_u24_e32 v9, 0x230, v9
	v_lshl_add_u32 v140, v14, 4, v9
	global_load_dwordx4 v[116:119], v10, s[12:13]
	v_add_u32_e32 v8, 0xa00, v0
	v_mul_u32_u24_e32 v9, 0xf0f1, v8
	v_lshrrev_b32_e32 v9, 21, v9
	v_mul_u32_u24_e32 v14, 34, v9
	v_sub_u32_e32 v14, v8, v14
	v_mul_u32_u24_e32 v10, 0x220, v9
	v_lshl_add_u32 v10, v14, 4, v10
	v_mul_u32_u24_e32 v9, 0x230, v9
	v_lshl_add_u32 v141, v14, 4, v9
	global_load_dwordx4 v[120:123], v10, s[12:13]
	v_add_u32_e32 v8, 0xc00, v0
	v_mul_u32_u24_e32 v9, 0xf0f1, v8
	v_lshrrev_b32_e32 v9, 21, v9
	v_mul_u32_u24_e32 v14, 34, v9
	v_sub_u32_e32 v14, v8, v14
	v_mul_u32_u24_e32 v10, 0x220, v9
	v_lshl_add_u32 v10, v14, 4, v10
	v_mul_u32_u24_e32 v9, 0x230, v9
	v_lshl_add_u32 v142, v14, 4, v9
	global_load_dwordx4 v[124:127], v10, s[12:13]
	v_add_u32_e32 v8, 0xe00, v0
	v_mul_u32_u24_e32 v9, 0xf0f1, v8
	v_lshrrev_b32_e32 v9, 21, v9
	v_mul_u32_u24_e32 v14, 34, v9
	v_sub_u32_e32 v14, v8, v14
	v_mul_u32_u24_e32 v10, 0x220, v9
	v_lshl_add_u32 v10, v14, 4, v10
	v_mul_u32_u24_e32 v9, 0x230, v9
	v_lshl_add_u32 v143, v14, 4, v9
	global_load_dwordx4 v[128:131], v10, s[12:13]
	v_cmp_gt_u32_e32 vcc, 0x100, v0
	s_and_saveexec_b64 s[58:59], vcc
	v_add_u32_e32 v8, 0x1000, v0
	v_mul_u32_u24_e32 v9, 0xf0f1, v8
	v_lshrrev_b32_e32 v9, 21, v9
	v_mul_u32_u24_e32 v14, 34, v9
	v_sub_u32_e32 v14, v8, v14
	v_mul_u32_u24_e32 v10, 0x220, v9
	v_lshl_add_u32 v10, v14, 4, v10
	v_mul_u32_u24_e32 v9, 0x230, v9
	v_lshl_add_u32 v144, v14, 4, v9
	global_load_dwordx4 v[132:135], v10, s[12:13]
	s_or_b64 exec, exec, s[58:59]
	s_waitcnt vmcnt(8)
	ds_write_b128 v136, v[100:103]
	s_waitcnt vmcnt(7)
	ds_write_b128 v137, v[104:107]
	s_waitcnt vmcnt(6)
	ds_write_b128 v138, v[108:111]
	s_waitcnt vmcnt(5)
	ds_write_b128 v139, v[112:115]
	s_waitcnt vmcnt(4)
	ds_write_b128 v140, v[116:119]
	s_waitcnt vmcnt(3)
	ds_write_b128 v141, v[120:123]
	s_waitcnt vmcnt(2)
	ds_write_b128 v142, v[124:127]
	s_waitcnt vmcnt(1)
	ds_write_b128 v143, v[128:131]
	s_waitcnt vmcnt(0)
	s_and_saveexec_b64 s[58:59], vcc
	ds_write_b128 v144, v[132:135]
	s_or_b64 exec, exec, s[58:59]
	s_mov_b32 s45, 2
